# baseline (speedup 1.0000x reference)
.Lh_no_out:
	s_cmp_eq_u32 s17, 0
	s_cselect_b32 s4, s4, s6
	s_cselect_b32 s5, s5, s7
	s_add_u32 s24, s8, s22
	s_addc_u32 s25, s9, 0
	s_add_u32 s4, s4, s21
	s_addc_u32 s5, s5, 0
	global_load_dwordx4 v[14:17], v18, s[24:25] nt
	global_load_dwordx4 v[2:5], v18, s[4:5] nt
	s_add_u32 s6, s4, 0x40000
	s_addc_u32 s7, s5, 0
	s_add_u32 s8, s4, 0x80000
	s_addc_u32 s9, s5, 0
	s_barrier
	global_load_dwordx4 v[6:9], v18, s[6:7] nt
	s_barrier
	global_load_dwordx4 v[10:13], v18, s[8:9] nt
	s_mul_i32 s46, s3, 0xc00
	s_add_u32 s46, s46, 0x8420
	v_lshl_add_u32 v26, v1, 2, s46
	v_and_b32_e32 v38, 15, v0
	s_mul_i32 s58, s17, 0x4200
	s_add_u32 s58, s58, 0x1e0
	v_lshl_add_u32 v38, v38, 2, s58
	v_add_u32_e32 v39, 0x1600, v38
	v_add_u32_e32 v40, 0x2c00, v38
	v_mov_b32_e32 v41, 0x41fc0000
	v_mov_b32_e32 v42, 0xbf38aa3b
	s_mov_b32 s48, 0x3f940000
	s_mov_b32 s51, 0x3fb8aa3b
	s_mov_b32 s42, 0
	s_mov_b32 s43, 0
	s_mov_b32 s44, 0x7fffffff
	s_mov_b32 s45, 0x7fffffff
	s_mov_b32 s47, 0
	s_mul_i32 s58, s3, 0x1600
	s_add_u32 s58, s58, 0x320
	v_lshl_add_u32 v44, v1, 6, s58
	v_bfe_u32 v45, v1, 2, 2
	v_lshlrev_b32_e32 v45, 4, v45
	v_xor_b32_e32 v46, 16, v45
	v_xor_b32_e32 v47, 32, v45
	v_xor_b32_e32 v48, 48, v45
	v_add_u32_e32 v45, v44, v45
	v_add_u32_e32 v46, v44, v46
	v_add_u32_e32 v47, v44, v47
	v_add_u32_e32 v48, v44, v48
	s_mul_i32 s58, s2, 0x600
	s_lshl_b32 s59, s3, 8
	s_add_u32 s58, s58, s59
	s_add_u32 s10, s10, s58
	s_addc_u32 s11, s11, 0
	v_lshlrev_b32_e32 v49, 2, v1
	s_lshl_b32 s58, s2, 2
	s_add_u32 s12, s12, s58
	s_addc_u32 s13, s13, 0
	s_setprio 3
	s_lshr_b32 s58, s3, 2
	s_cmp_eq_u32 s58, 0
	s_cbranch_scc1 .Lh_nostagger
	s_sleep 2
	s_cmp_eq_u32 s58, 1
	s_cbranch_scc1 .Lh_nostagger
	s_sleep 2
	s_cmp_eq_u32 s58, 2
	s_cbranch_scc1 .Lh_nostagger
	s_sleep 2
